# v30 + first two chunks per wave assigned statically (no initial LDS atomics)
# speedup vs baseline: 1.0206x; 1.0206x over previous
_Z7vq_mainPKfPKiS0_PfPhPdPi:
	s_load_dwordx4 s[4:7], s[0:1], 0x0
	s_load_dwordx2 s[22:23], s[0:1], 0x10
	s_load_dwordx2 s[20:21], s[0:1], 0x18
	s_load_dwordx4 s[12:15], s[0:1], 0x20
	s_load_dwordx2 s[10:11], s[0:1], 0x30
	s_and_b32 s3, s2, 7
	s_lshl_b32 s3, s3, 6
	s_lshr_b32 s16, s2, 3
	s_add_i32 s16, s16, s3
	s_lshr_b32 s18, s16, 5
	s_mov_b32 s19, 0
	s_and_b32 s28, s16, 31
	s_lshl_b32 s28, s28, 4
	s_add_i32 s29, s28, 1
	v_readfirstlane_b32 s17, v0
	v_and_b32_e32 v1, 63, v0
	v_lshlrev_b32_e32 v66, 4, v0
	s_lshr_b32 s17, s17, 6
	s_lshl_b32 s24, s17, 4
	s_lshl_b32 s30, s18, 15
	s_lshl_b32 s31, s18, 23
	v_add_u32_e32 v67, 0x1000, v66
	v_add_u32_e32 v68, 0x2000, v66
	v_add_u32_e32 v69, 0x3000, v66
	v_add_u32_e32 v70, 0x4000, v66
	v_add_u32_e32 v71, 0x5000, v66
	v_add_u32_e32 v72, 0x6000, v66
	v_add_u32_e32 v73, 0x7000, v66
	s_waitcnt lgkmcnt(0)
	s_add_u32 s34, s6, s30
	s_addc_u32 s35, s7, 0
	s_add_u32 s32, s4, s31
	s_addc_u32 s33, s5, 0
	global_load_dwordx4 v[74:77], v66, s[34:35]
	global_load_dwordx4 v[78:81], v67, s[34:35]
	global_load_dwordx4 v[82:85], v68, s[34:35]
	global_load_dwordx4 v[86:89], v69, s[34:35]
	global_load_dwordx4 v[90:93], v70, s[34:35]
	global_load_dwordx4 v[94:97], v71, s[34:35]
	global_load_dwordx4 v[98:101], v72, s[34:35]
	global_load_dwordx4 v[102:105], v73, s[34:35]
	v_and_b32_e32 v150, 15, v0
	v_or_b32_e32 v150, s24, v150
	v_and_b32_e32 v151, 48, v0
	v_lshl_or_b32 v150, v150, 10, v151
	global_load_dwordx4 v[62:65], v150, s[22:23] offset:0
	global_load_dwordx4 v[58:61], v150, s[22:23] offset:64
	global_load_dwordx4 v[54:57], v150, s[22:23] offset:128
	global_load_dwordx4 v[50:53], v150, s[22:23] offset:192
	global_load_dwordx4 v[46:49], v150, s[22:23] offset:256
	global_load_dwordx4 v[42:45], v150, s[22:23] offset:320
	global_load_dwordx4 v[38:41], v150, s[22:23] offset:384
	global_load_dwordx4 v[34:37], v150, s[22:23] offset:448
	global_load_dwordx4 v[30:33], v150, s[22:23] offset:512
	global_load_dwordx4 v[26:29], v150, s[22:23] offset:576
	global_load_dwordx4 v[22:25], v150, s[22:23] offset:640
	global_load_dwordx4 v[18:21], v150, s[22:23] offset:704
	global_load_dwordx4 v[14:17], v150, s[22:23] offset:768
	global_load_dwordx4 v[10:13], v150, s[22:23] offset:832
	global_load_dwordx4 v[6:9], v150, s[22:23] offset:896
	global_load_dwordx4 v[2:5], v150, s[22:23] offset:960
	v_mov_b32_e32 v142, 1
	v_mov_b32_e32 v143, 4
	v_mov_b32_e32 v144, 0x11100
	v_lshlrev_b32_e32 v145, 8, v0
	v_lshlrev_b32_e32 v148, 3, v0
	v_mov_b32_e32 v152, 0
	v_mov_b32_e32 v153, 0
	ds_write_b64 v148, v[152:153] offset:32768
	ds_write_b64 v148, v[152:153] offset:34832
	ds_write_b64 v148, v[152:153] offset:36896
	ds_write_b64 v148, v[152:153] offset:38960
	ds_write_b64 v148, v[152:153] offset:41024
	ds_write_b64 v148, v[152:153] offset:43088
	ds_write_b64 v148, v[152:153] offset:45152
	ds_write_b64 v148, v[152:153] offset:47216
	ds_write_b64 v148, v[152:153] offset:49280
	ds_write_b64 v148, v[152:153] offset:51344
	ds_write_b64 v148, v[152:153] offset:53408
	ds_write_b64 v148, v[152:153] offset:55472
	ds_write_b64 v148, v[152:153] offset:57536
	ds_write_b64 v148, v[152:153] offset:59600
	ds_write_b64 v148, v[152:153] offset:61664
	ds_write_b64 v148, v[152:153] offset:63728
	v_cmp_gt_u32_e32 vcc, 16, v0
	s_and_saveexec_b64 s[30:31], vcc
	v_lshl_add_u32 v151, v0, 2, v144
	ds_write_b32 v151, v152
	v_mov_b32_e32 v150, 0x11540
	v_mov_b32_e32 v149, 8
	ds_write_b32 v150, v149
	s_mov_b64 exec, s[30:31]
	s_waitcnt lgkmcnt(0)
	s_barrier
	s_waitcnt vmcnt(16)
	v_subrev_u32_e32 v74, s29, v74
	v_subrev_u32_e32 v75, s29, v75
	v_subrev_u32_e32 v76, s29, v76
	v_subrev_u32_e32 v77, s29, v77
	v_subrev_u32_e32 v78, s29, v78
	v_subrev_u32_e32 v79, s29, v79
	v_subrev_u32_e32 v80, s29, v80
	v_subrev_u32_e32 v81, s29, v81
	v_subrev_u32_e32 v82, s29, v82
	v_subrev_u32_e32 v83, s29, v83
	v_subrev_u32_e32 v84, s29, v84
	v_subrev_u32_e32 v85, s29, v85
	v_subrev_u32_e32 v86, s29, v86
	v_subrev_u32_e32 v87, s29, v87
	v_subrev_u32_e32 v88, s29, v88
	v_subrev_u32_e32 v89, s29, v89
	v_subrev_u32_e32 v90, s29, v90
	v_subrev_u32_e32 v91, s29, v91
	v_subrev_u32_e32 v92, s29, v92
	v_subrev_u32_e32 v93, s29, v93
	v_subrev_u32_e32 v94, s29, v94
	v_subrev_u32_e32 v95, s29, v95
	v_subrev_u32_e32 v96, s29, v96
	v_subrev_u32_e32 v97, s29, v97
	v_subrev_u32_e32 v98, s29, v98
	v_subrev_u32_e32 v99, s29, v99
	v_subrev_u32_e32 v100, s29, v100
	v_subrev_u32_e32 v101, s29, v101
	v_subrev_u32_e32 v102, s29, v102
	v_subrev_u32_e32 v103, s29, v103
	v_subrev_u32_e32 v104, s29, v104
	v_subrev_u32_e32 v105, s29, v105
	v_cmp_gt_u32_e64 s[36:37], 16, v74
	v_cmp_gt_u32_e64 s[38:39], 16, v75
	v_cmp_gt_u32_e64 s[40:41], 16, v76
	v_cmp_gt_u32_e64 s[42:43], 16, v77
	v_cmp_gt_u32_e64 s[44:45], 16, v78
	v_cmp_gt_u32_e64 s[46:47], 16, v79
	v_cmp_gt_u32_e64 s[48:49], 16, v80
	v_cmp_gt_u32_e64 s[50:51], 16, v81
	v_cmp_gt_u32_e64 s[52:53], 16, v82
	v_cmp_gt_u32_e64 s[54:55], 16, v83
	v_cmp_gt_u32_e64 s[56:57], 16, v84
	v_cmp_gt_u32_e64 s[58:59], 16, v85
	v_cmp_gt_u32_e64 s[60:61], 16, v86
	v_cmp_gt_u32_e64 s[62:63], 16, v87
	v_cmp_gt_u32_e64 s[64:65], 16, v88
	v_cmp_gt_u32_e64 s[66:67], 16, v89
	v_cmp_gt_u32_e64 s[68:69], 16, v90
	v_cmp_gt_u32_e64 s[70:71], 16, v91
	v_cmp_gt_u32_e64 s[72:73], 16, v92
	v_cmp_gt_u32_e64 s[74:75], 16, v93
	v_cmp_gt_u32_e64 s[76:77], 16, v94
	v_cmp_gt_u32_e64 s[78:79], 16, v95
	v_cmp_gt_u32_e64 s[80:81], 16, v96
	v_cmp_gt_u32_e64 s[82:83], 16, v97
	v_cmp_gt_u32_e64 s[84:85], 16, v98
	v_cmp_gt_u32_e64 s[86:87], 16, v99
	v_cmp_gt_u32_e64 s[88:89], 16, v100
	v_cmp_gt_u32_e64 s[90:91], 16, v101
	v_cmp_gt_u32_e64 s[92:93], 16, v102
	v_cmp_gt_u32_e64 s[94:95], 16, v103
	v_cmp_gt_u32_e64 s[96:97], 16, v104
	v_cmp_gt_u32_e64 s[98:99], 16, v105
	s_mov_b64 exec, s[36:37]
	v_lshl_add_u32 v74, v74, 2, v144
	ds_add_u32 v74, v142
	s_mov_b64 exec, s[38:39]
	v_lshl_add_u32 v75, v75, 2, v144
	ds_add_u32 v75, v142
	s_mov_b64 exec, s[40:41]
	v_lshl_add_u32 v76, v76, 2, v144
	ds_add_u32 v76, v142
	s_mov_b64 exec, s[42:43]
	v_lshl_add_u32 v77, v77, 2, v144
	ds_add_u32 v77, v142
	s_mov_b64 exec, s[44:45]
	v_lshl_add_u32 v78, v78, 2, v144
	ds_add_u32 v78, v142
	s_mov_b64 exec, s[46:47]
	v_lshl_add_u32 v79, v79, 2, v144
	ds_add_u32 v79, v142
	s_mov_b64 exec, s[48:49]
	v_lshl_add_u32 v80, v80, 2, v144
	ds_add_u32 v80, v142
	s_mov_b64 exec, s[50:51]
	v_lshl_add_u32 v81, v81, 2, v144
	ds_add_u32 v81, v142
	s_mov_b64 exec, s[52:53]
	v_lshl_add_u32 v82, v82, 2, v144
	ds_add_u32 v82, v142
	s_mov_b64 exec, s[54:55]
	v_lshl_add_u32 v83, v83, 2, v144
	ds_add_u32 v83, v142
	s_mov_b64 exec, s[56:57]
	v_lshl_add_u32 v84, v84, 2, v144
	ds_add_u32 v84, v142
	s_mov_b64 exec, s[58:59]
	v_lshl_add_u32 v85, v85, 2, v144
	ds_add_u32 v85, v142
	s_mov_b64 exec, s[60:61]
	v_lshl_add_u32 v86, v86, 2, v144
	ds_add_u32 v86, v142
	s_mov_b64 exec, s[62:63]
	v_lshl_add_u32 v87, v87, 2, v144
	ds_add_u32 v87, v142
	s_mov_b64 exec, s[64:65]
	v_lshl_add_u32 v88, v88, 2, v144
	ds_add_u32 v88, v142
	s_mov_b64 exec, s[66:67]
	v_lshl_add_u32 v89, v89, 2, v144
	ds_add_u32 v89, v142
	s_mov_b64 exec, s[68:69]
	v_lshl_add_u32 v90, v90, 2, v144
	ds_add_u32 v90, v142
	s_mov_b64 exec, s[70:71]
	v_lshl_add_u32 v91, v91, 2, v144
	ds_add_u32 v91, v142
	s_mov_b64 exec, s[72:73]
	v_lshl_add_u32 v92, v92, 2, v144
	ds_add_u32 v92, v142
	s_mov_b64 exec, s[74:75]
	v_lshl_add_u32 v93, v93, 2, v144
	ds_add_u32 v93, v142
	s_mov_b64 exec, s[76:77]
	v_lshl_add_u32 v94, v94, 2, v144
	ds_add_u32 v94, v142
	s_mov_b64 exec, s[78:79]
	v_lshl_add_u32 v95, v95, 2, v144
	ds_add_u32 v95, v142
	s_mov_b64 exec, s[80:81]
	v_lshl_add_u32 v96, v96, 2, v144
	ds_add_u32 v96, v142
	s_mov_b64 exec, s[82:83]
	v_lshl_add_u32 v97, v97, 2, v144
	ds_add_u32 v97, v142
	s_mov_b64 exec, s[84:85]
	v_lshl_add_u32 v98, v98, 2, v144
	ds_add_u32 v98, v142
	s_mov_b64 exec, s[86:87]
	v_lshl_add_u32 v99, v99, 2, v144
	ds_add_u32 v99, v142
	s_mov_b64 exec, s[88:89]
	v_lshl_add_u32 v100, v100, 2, v144
	ds_add_u32 v100, v142
	s_mov_b64 exec, s[90:91]
	v_lshl_add_u32 v101, v101, 2, v144
	ds_add_u32 v101, v142
	s_mov_b64 exec, s[92:93]
	v_lshl_add_u32 v102, v102, 2, v144
	ds_add_u32 v102, v142
	s_mov_b64 exec, s[94:95]
	v_lshl_add_u32 v103, v103, 2, v144
	ds_add_u32 v103, v142
	s_mov_b64 exec, s[96:97]
	v_lshl_add_u32 v104, v104, 2, v144
	ds_add_u32 v104, v142
	s_mov_b64 exec, s[98:99]
	v_lshl_add_u32 v105, v105, 2, v144
	ds_add_u32 v105, v142
	s_mov_b64 exec, -1
	s_waitcnt lgkmcnt(0)
	s_barrier
	v_and_b32_e32 v67, 15, v0
	v_lshl_add_u32 v67, v67, 2, v144
	ds_read_b32 v68, v67
	s_waitcnt lgkmcnt(0)
	v_mov_b32_e32 v69, v68
	s_nop 1
	v_add_u32_dpp v69, v69, v69 row_shr:1 row_mask:0xf bank_mask:0xf bound_ctrl:1
	s_nop 1
	v_add_u32_dpp v69, v69, v69 row_shr:2 row_mask:0xf bank_mask:0xf bound_ctrl:1
	s_nop 1
	v_add_u32_dpp v69, v69, v69 row_shr:4 row_mask:0xf bank_mask:0xf bound_ctrl:1
	s_nop 1
	v_add_u32_dpp v69, v69, v69 row_shr:8 row_mask:0xf bank_mask:0xf bound_ctrl:1
	s_nop 1
	v_sub_u32_e32 v70, v69, v68
	v_lshlrev_b32_e32 v70, 2, v70
	v_readlane_b32 s8, v69, 15
	s_cmp_lg_u32 s17, 0
	s_cbranch_scc1 .Lfront_nocursor
	v_cmp_gt_u32_e32 vcc, 16, v1
	s_and_saveexec_b64 s[30:31], vcc
	ds_write_b32 v67, v70 offset:64
	s_mov_b64 exec, s[30:31]
.Lfront_nocursor:
	s_waitcnt lgkmcnt(0)
	s_barrier
	s_mov_b64 exec, s[36:37]
	ds_add_rtn_u32 v106, v74, v143 offset:64
	s_mov_b64 exec, s[38:39]
	ds_add_rtn_u32 v107, v75, v143 offset:64
	s_mov_b64 exec, s[40:41]
	ds_add_rtn_u32 v108, v76, v143 offset:64
	s_mov_b64 exec, s[42:43]
	ds_add_rtn_u32 v109, v77, v143 offset:64
	s_mov_b64 exec, s[44:45]
	ds_add_rtn_u32 v110, v78, v143 offset:64
	s_mov_b64 exec, s[46:47]
	ds_add_rtn_u32 v111, v79, v143 offset:64
	s_mov_b64 exec, s[48:49]
	ds_add_rtn_u32 v112, v80, v143 offset:64
	s_mov_b64 exec, s[50:51]
	ds_add_rtn_u32 v113, v81, v143 offset:64
	s_mov_b64 exec, s[52:53]
	ds_add_rtn_u32 v114, v82, v143 offset:64
	s_mov_b64 exec, s[54:55]
	ds_add_rtn_u32 v115, v83, v143 offset:64
	s_mov_b64 exec, s[56:57]
	ds_add_rtn_u32 v116, v84, v143 offset:64
	s_mov_b64 exec, s[58:59]
	ds_add_rtn_u32 v117, v85, v143 offset:64
	s_mov_b64 exec, s[60:61]
	ds_add_rtn_u32 v118, v86, v143 offset:64
	s_mov_b64 exec, s[62:63]
	ds_add_rtn_u32 v119, v87, v143 offset:64
	s_mov_b64 exec, s[64:65]
	ds_add_rtn_u32 v120, v88, v143 offset:64
	s_mov_b64 exec, s[66:67]
	ds_add_rtn_u32 v121, v89, v143 offset:64
	s_mov_b64 exec, s[68:69]
	ds_add_rtn_u32 v122, v90, v143 offset:64
	s_mov_b64 exec, s[70:71]
	ds_add_rtn_u32 v123, v91, v143 offset:64
	s_mov_b64 exec, s[72:73]
	ds_add_rtn_u32 v124, v92, v143 offset:64
	s_mov_b64 exec, s[74:75]
	ds_add_rtn_u32 v125, v93, v143 offset:64
	s_mov_b64 exec, s[76:77]
	ds_add_rtn_u32 v126, v94, v143 offset:64
	s_mov_b64 exec, s[78:79]
	ds_add_rtn_u32 v127, v95, v143 offset:64
	s_mov_b64 exec, s[80:81]
	ds_add_rtn_u32 v128, v96, v143 offset:64
	s_mov_b64 exec, s[82:83]
	ds_add_rtn_u32 v129, v97, v143 offset:64
	s_mov_b64 exec, s[84:85]
	ds_add_rtn_u32 v130, v98, v143 offset:64
	s_mov_b64 exec, s[86:87]
	ds_add_rtn_u32 v131, v99, v143 offset:64
	s_mov_b64 exec, s[88:89]
	ds_add_rtn_u32 v132, v100, v143 offset:64
	s_mov_b64 exec, s[90:91]
	ds_add_rtn_u32 v133, v101, v143 offset:64
	s_mov_b64 exec, s[92:93]
	ds_add_rtn_u32 v134, v102, v143 offset:64
	s_mov_b64 exec, s[94:95]
	ds_add_rtn_u32 v135, v103, v143 offset:64
	s_mov_b64 exec, s[96:97]
	ds_add_rtn_u32 v136, v104, v143 offset:64
	s_mov_b64 exec, s[98:99]
	ds_add_rtn_u32 v137, v105, v143 offset:64
	s_mov_b64 exec, -1
	v_add_u32_e32 v146, 0x0, v145
	v_and_or_b32 v146, v74, 60, v146
	s_waitcnt lgkmcnt(0)
	s_mov_b64 exec, s[36:37]
	ds_write_b32 v106, v146
	s_mov_b64 exec, -1
	v_add_u32_e32 v147, 0x40, v145
	v_and_or_b32 v147, v75, 60, v147
	s_mov_b64 exec, s[38:39]
	ds_write_b32 v107, v147
	s_mov_b64 exec, -1
	v_add_u32_e32 v146, 0x80, v145
	v_and_or_b32 v146, v76, 60, v146
	s_mov_b64 exec, s[40:41]
	ds_write_b32 v108, v146
	s_mov_b64 exec, -1
	v_add_u32_e32 v147, 0xc0, v145
	v_and_or_b32 v147, v77, 60, v147
	s_mov_b64 exec, s[42:43]
	ds_write_b32 v109, v147
	s_mov_b64 exec, -1
	v_add_u32_e32 v146, 0x10000, v145
	v_and_or_b32 v146, v78, 60, v146
	s_mov_b64 exec, s[44:45]
	ds_write_b32 v110, v146
	s_mov_b64 exec, -1
	v_add_u32_e32 v147, 0x10040, v145
	v_and_or_b32 v147, v79, 60, v147
	s_mov_b64 exec, s[46:47]
	ds_write_b32 v111, v147
	s_mov_b64 exec, -1
	v_add_u32_e32 v146, 0x10080, v145
	v_and_or_b32 v146, v80, 60, v146
	s_mov_b64 exec, s[48:49]
	ds_write_b32 v112, v146
	s_mov_b64 exec, -1
	v_add_u32_e32 v147, 0x100c0, v145
	v_and_or_b32 v147, v81, 60, v147
	s_mov_b64 exec, s[50:51]
	ds_write_b32 v113, v147
	s_mov_b64 exec, -1
	v_add_u32_e32 v146, 0x20000, v145
	v_and_or_b32 v146, v82, 60, v146
	s_mov_b64 exec, s[52:53]
	ds_write_b32 v114, v146
	s_mov_b64 exec, -1
	v_add_u32_e32 v147, 0x20040, v145
	v_and_or_b32 v147, v83, 60, v147
	s_mov_b64 exec, s[54:55]
	ds_write_b32 v115, v147
	s_mov_b64 exec, -1
	v_add_u32_e32 v146, 0x20080, v145
	v_and_or_b32 v146, v84, 60, v146
	s_mov_b64 exec, s[56:57]
	ds_write_b32 v116, v146
	s_mov_b64 exec, -1
	v_add_u32_e32 v147, 0x200c0, v145
	v_and_or_b32 v147, v85, 60, v147
	s_mov_b64 exec, s[58:59]
	ds_write_b32 v117, v147
	s_mov_b64 exec, -1
	v_add_u32_e32 v146, 0x30000, v145
	v_and_or_b32 v146, v86, 60, v146
	s_mov_b64 exec, s[60:61]
	ds_write_b32 v118, v146
	s_mov_b64 exec, -1
	v_add_u32_e32 v147, 0x30040, v145
	v_and_or_b32 v147, v87, 60, v147
	s_mov_b64 exec, s[62:63]
	ds_write_b32 v119, v147
	s_mov_b64 exec, -1
	v_add_u32_e32 v146, 0x30080, v145
	v_and_or_b32 v146, v88, 60, v146
	s_mov_b64 exec, s[64:65]
	ds_write_b32 v120, v146
	s_mov_b64 exec, -1
	v_add_u32_e32 v147, 0x300c0, v145
	v_and_or_b32 v147, v89, 60, v147
	s_mov_b64 exec, s[66:67]
	ds_write_b32 v121, v147
	s_mov_b64 exec, -1
	v_add_u32_e32 v146, 0x40000, v145
	v_and_or_b32 v146, v90, 60, v146
	s_mov_b64 exec, s[68:69]
	ds_write_b32 v122, v146
	s_mov_b64 exec, -1
	v_add_u32_e32 v147, 0x40040, v145
	v_and_or_b32 v147, v91, 60, v147
	s_mov_b64 exec, s[70:71]
	ds_write_b32 v123, v147
	s_mov_b64 exec, -1
	v_add_u32_e32 v146, 0x40080, v145
	v_and_or_b32 v146, v92, 60, v146
	s_mov_b64 exec, s[72:73]
	ds_write_b32 v124, v146
	s_mov_b64 exec, -1
	v_add_u32_e32 v147, 0x400c0, v145
	v_and_or_b32 v147, v93, 60, v147
	s_mov_b64 exec, s[74:75]
	ds_write_b32 v125, v147
	s_mov_b64 exec, -1
	v_add_u32_e32 v146, 0x50000, v145
	v_and_or_b32 v146, v94, 60, v146
	s_mov_b64 exec, s[76:77]
	ds_write_b32 v126, v146
	s_mov_b64 exec, -1
	v_add_u32_e32 v147, 0x50040, v145
	v_and_or_b32 v147, v95, 60, v147
	s_mov_b64 exec, s[78:79]
	ds_write_b32 v127, v147
	s_mov_b64 exec, -1
	v_add_u32_e32 v146, 0x50080, v145
	v_and_or_b32 v146, v96, 60, v146
	s_mov_b64 exec, s[80:81]
	ds_write_b32 v128, v146
	s_mov_b64 exec, -1
	v_add_u32_e32 v147, 0x500c0, v145
	v_and_or_b32 v147, v97, 60, v147
	s_mov_b64 exec, s[82:83]
	ds_write_b32 v129, v147
	s_mov_b64 exec, -1
	v_add_u32_e32 v146, 0x60000, v145
	v_and_or_b32 v146, v98, 60, v146
	s_mov_b64 exec, s[84:85]
	ds_write_b32 v130, v146
	s_mov_b64 exec, -1
	v_add_u32_e32 v147, 0x60040, v145
	v_and_or_b32 v147, v99, 60, v147
	s_mov_b64 exec, s[86:87]
	ds_write_b32 v131, v147
	s_mov_b64 exec, -1
	v_add_u32_e32 v146, 0x60080, v145
	v_and_or_b32 v146, v100, 60, v146
	s_mov_b64 exec, s[88:89]
	ds_write_b32 v132, v146
	s_mov_b64 exec, -1
	v_add_u32_e32 v147, 0x600c0, v145
	v_and_or_b32 v147, v101, 60, v147
	s_mov_b64 exec, s[90:91]
	ds_write_b32 v133, v147
	s_mov_b64 exec, -1
	v_add_u32_e32 v146, 0x70000, v145
	v_and_or_b32 v146, v102, 60, v146
	s_mov_b64 exec, s[92:93]
	ds_write_b32 v134, v146
	s_mov_b64 exec, -1
	v_add_u32_e32 v147, 0x70040, v145
	v_and_or_b32 v147, v103, 60, v147
	s_mov_b64 exec, s[94:95]
	ds_write_b32 v135, v147
	s_mov_b64 exec, -1
	v_add_u32_e32 v146, 0x70080, v145
	v_and_or_b32 v146, v104, 60, v146
	s_mov_b64 exec, s[96:97]
	ds_write_b32 v136, v146
	s_mov_b64 exec, -1
	v_add_u32_e32 v147, 0x700c0, v145
	v_and_or_b32 v147, v105, 60, v147
	s_mov_b64 exec, s[98:99]
	ds_write_b32 v137, v147
	s_mov_b64 exec, -1
	s_waitcnt lgkmcnt(0)
	s_barrier
	s_add_i32 s53, s8, 7
	s_lshr_b32 s53, s53, 3
	v_lshlrev_b32_e32 v218, 4, v1
	v_lshlrev_b32_e32 v219, 3, v1
	v_mov_b32_e32 v223, 0x11540
	v_and_b32_e32 v221, 15, v1
	v_mov_b32_e32 v200, 0
	v_mov_b32_e32 v201, 0
	v_mov_b32_e32 v202, 0
	v_mov_b32_e32 v203, 0
	v_mov_b32_e32 v204, 0
	v_mov_b32_e32 v205, 0
	v_mov_b32_e32 v206, 0
	v_mov_b32_e32 v207, 0
	s_mov_b32 s50, -1
	s_mov_b32 s54, s17
	s_add_i32 s55, s17, 4
	s_cmp_ge_u32 s54, s53
	s_cbranch_scc1 .Lg_nochunk
	s_lshl_b32 s46, s54, 3
	v_add_u32_e32 v220, s46, v221
	v_cmp_gt_u32_e32 vcc, s8, v220
	v_lshlrev_b32_e32 v220, 2, v220
	ds_read_b32 v216, v220
	s_waitcnt lgkmcnt(0)
	v_cndmask_b32_e32 v216, 1, v216, vcc
	s_nop 1
	v_readlane_b32 s50, v216, 0
	s_bfe_u32 s50, s50, 0x40002
	v_readlane_b32 s40, v216, 0
	s_bfe_u32 s60, s40, 0x40002
	s_bitcmp1_b32 s40, 0
	s_cselect_b32 s60, 16, s60
	s_and_b32 s40, s40, 0xffffffc0
	s_lshl_b32 s40, s40, 4
	s_add_u32 s42, s32, s40
	s_addc_u32 s43, s33, 0
	global_load_dwordx4 v[66:69], v218, s[42:43] nt
	v_readlane_b32 s40, v216, 1
	s_bfe_u32 s61, s40, 0x40002
	s_bitcmp1_b32 s40, 0
	s_cselect_b32 s61, 16, s61
	s_and_b32 s40, s40, 0xffffffc0
	s_lshl_b32 s40, s40, 4
	s_add_u32 s42, s32, s40
	s_addc_u32 s43, s33, 0
	global_load_dwordx4 v[70:73], v218, s[42:43] nt
	v_readlane_b32 s40, v216, 2
	s_bfe_u32 s62, s40, 0x40002
	s_bitcmp1_b32 s40, 0
	s_cselect_b32 s62, 16, s62
	s_and_b32 s40, s40, 0xffffffc0
	s_lshl_b32 s40, s40, 4
	s_add_u32 s42, s32, s40
	s_addc_u32 s43, s33, 0
	global_load_dwordx4 v[74:77], v218, s[42:43] nt
	v_readlane_b32 s40, v216, 3
	s_bfe_u32 s63, s40, 0x40002
	s_bitcmp1_b32 s40, 0
	s_cselect_b32 s63, 16, s63
	s_and_b32 s40, s40, 0xffffffc0
	s_lshl_b32 s40, s40, 4
	s_add_u32 s42, s32, s40
	s_addc_u32 s43, s33, 0
	global_load_dwordx4 v[78:81], v218, s[42:43] nt
	v_readlane_b32 s40, v216, 4
	s_bfe_u32 s64, s40, 0x40002
	s_bitcmp1_b32 s40, 0
	s_cselect_b32 s64, 16, s64
	s_and_b32 s40, s40, 0xffffffc0
	s_lshl_b32 s40, s40, 4
	s_add_u32 s42, s32, s40
	s_addc_u32 s43, s33, 0
	global_load_dwordx4 v[82:85], v218, s[42:43] nt
	v_readlane_b32 s40, v216, 5
	s_bfe_u32 s65, s40, 0x40002
	s_bitcmp1_b32 s40, 0
	s_cselect_b32 s65, 16, s65
	s_and_b32 s40, s40, 0xffffffc0
	s_lshl_b32 s40, s40, 4
	s_add_u32 s42, s32, s40
	s_addc_u32 s43, s33, 0
	global_load_dwordx4 v[86:89], v218, s[42:43] nt
	v_readlane_b32 s40, v216, 6
	s_bfe_u32 s66, s40, 0x40002
	s_bitcmp1_b32 s40, 0
	s_cselect_b32 s66, 16, s66
	s_and_b32 s40, s40, 0xffffffc0
	s_lshl_b32 s40, s40, 4
	s_add_u32 s42, s32, s40
	s_addc_u32 s43, s33, 0
	global_load_dwordx4 v[90:93], v218, s[42:43] nt
	v_readlane_b32 s40, v216, 7
	s_bfe_u32 s67, s40, 0x40002
	s_bitcmp1_b32 s40, 0
	s_cselect_b32 s67, 16, s67
	s_and_b32 s40, s40, 0xffffffc0
	s_lshl_b32 s40, s40, 4
	s_add_u32 s42, s32, s40
	s_addc_u32 s43, s33, 0
	global_load_dwordx4 v[94:97], v218, s[42:43] nt
	s_cmp_ge_u32 s55, s53
	s_cbranch_scc1 .Lg_noB
	s_lshl_b32 s46, s55, 3
	v_add_u32_e32 v220, s46, v221
	v_cmp_gt_u32_e32 vcc, s8, v220
	v_lshlrev_b32_e32 v220, 2, v220
	ds_read_b32 v217, v220
	s_waitcnt lgkmcnt(0)
	v_cndmask_b32_e32 v217, 1, v217, vcc
	s_nop 1
	v_readlane_b32 s40, v217, 0
	s_bfe_u32 s68, s40, 0x40002
	s_bitcmp1_b32 s40, 0
	s_cselect_b32 s68, 16, s68
	s_and_b32 s40, s40, 0xffffffc0
	s_lshl_b32 s40, s40, 4
	s_add_u32 s42, s32, s40
	s_addc_u32 s43, s33, 0
	global_load_dwordx4 v[98:101], v218, s[42:43] nt
	v_readlane_b32 s40, v217, 1
	s_bfe_u32 s69, s40, 0x40002
	s_bitcmp1_b32 s40, 0
	s_cselect_b32 s69, 16, s69
	s_and_b32 s40, s40, 0xffffffc0
	s_lshl_b32 s40, s40, 4
	s_add_u32 s42, s32, s40
	s_addc_u32 s43, s33, 0
	global_load_dwordx4 v[102:105], v218, s[42:43] nt
	v_readlane_b32 s40, v217, 2
	s_bfe_u32 s70, s40, 0x40002
	s_bitcmp1_b32 s40, 0
	s_cselect_b32 s70, 16, s70
	s_and_b32 s40, s40, 0xffffffc0
	s_lshl_b32 s40, s40, 4
	s_add_u32 s42, s32, s40
	s_addc_u32 s43, s33, 0
	global_load_dwordx4 v[106:109], v218, s[42:43] nt
	v_readlane_b32 s40, v217, 3
	s_bfe_u32 s71, s40, 0x40002
	s_bitcmp1_b32 s40, 0
	s_cselect_b32 s71, 16, s71
	s_and_b32 s40, s40, 0xffffffc0
	s_lshl_b32 s40, s40, 4
	s_add_u32 s42, s32, s40
	s_addc_u32 s43, s33, 0
	global_load_dwordx4 v[110:113], v218, s[42:43] nt
	v_readlane_b32 s40, v217, 4
	s_bfe_u32 s72, s40, 0x40002
	s_bitcmp1_b32 s40, 0
	s_cselect_b32 s72, 16, s72
	s_and_b32 s40, s40, 0xffffffc0
	s_lshl_b32 s40, s40, 4
	s_add_u32 s42, s32, s40
	s_addc_u32 s43, s33, 0
	global_load_dwordx4 v[114:117], v218, s[42:43] nt
	v_readlane_b32 s40, v217, 5
	s_bfe_u32 s73, s40, 0x40002
	s_bitcmp1_b32 s40, 0
	s_cselect_b32 s73, 16, s73
	s_and_b32 s40, s40, 0xffffffc0
	s_lshl_b32 s40, s40, 4
	s_add_u32 s42, s32, s40
	s_addc_u32 s43, s33, 0
	global_load_dwordx4 v[118:121], v218, s[42:43] nt
	v_readlane_b32 s40, v217, 6
	s_bfe_u32 s74, s40, 0x40002
	s_bitcmp1_b32 s40, 0
	s_cselect_b32 s74, 16, s74
	s_and_b32 s40, s40, 0xffffffc0
	s_lshl_b32 s40, s40, 4
	s_add_u32 s42, s32, s40
	s_addc_u32 s43, s33, 0
	global_load_dwordx4 v[122:125], v218, s[42:43] nt
	v_readlane_b32 s40, v217, 7
	s_bfe_u32 s75, s40, 0x40002
	s_bitcmp1_b32 s40, 0
	s_cselect_b32 s75, 16, s75
	s_and_b32 s40, s40, 0xffffffc0
	s_lshl_b32 s40, s40, 4
	s_add_u32 s42, s32, s40
	s_addc_u32 s43, s33, 0
	global_load_dwordx4 v[126:129], v218, s[42:43] nt

.Lg_noB:
.Lg_drainA:
	s_waitcnt vmcnt(7)
	s_cmp_eq_u32 s60, 16
	s_cbranch_scc1 .Lc_A0_skip0
	s_cmp_lg_u32 s60, s50
	s_cbranch_scc1 .Lc_A0_flush0

.Lc_B0_skip15:
.Lg_fin:
	s_mul_i32 s42, s50, 0x810
	v_add_u32_e32 v220, s42, v219
	ds_add_f64 v220, v[200:201] offset:32768
	ds_add_f64 v220, v[202:203] offset:33280
	ds_add_f64 v220, v[204:205] offset:33792
	ds_add_f64 v220, v[206:207] offset:34304
	s_branch .Lg_alldone
.Lg_nochunk:
	s_branch .Lg_alldone
.Lc_A8_flush0:
	s_mul_i32 s42, s50, 0x810
	v_add_u32_e32 v220, s42, v219
	ds_add_f64 v220, v[200:201] offset:32768
	ds_add_f64 v220, v[202:203] offset:33280
	ds_add_f64 v220, v[204:205] offset:33792
	ds_add_f64 v220, v[206:207] offset:34304
	v_mov_b32_e32 v200, 0
	v_mov_b32_e32 v201, 0
	v_mov_b32_e32 v202, 0
	v_mov_b32_e32 v203, 0
	v_mov_b32_e32 v204, 0
	v_mov_b32_e32 v205, 0
	v_mov_b32_e32 v206, 0
	v_mov_b32_e32 v207, 0
	s_mov_b32 s50, s60
	s_branch .Lc_A8_cont0

.Lg_alldone:
	s_waitcnt vmcnt(0)
	s_waitcnt vmcnt(16)
	v_mul_f32_e32 v150, v62, v62
	v_mul_f32_e32 v151, v63, v63
	v_mul_f32_e32 v152, v64, v64
	v_mul_f32_e32 v153, v65, v65
	v_fmac_f32_e32 v150, v58, v58
	v_fmac_f32_e32 v151, v59, v59
	v_fmac_f32_e32 v152, v60, v60
	v_fmac_f32_e32 v153, v61, v61
	v_fmac_f32_e32 v150, v54, v54
	v_fmac_f32_e32 v151, v55, v55
	v_fmac_f32_e32 v152, v56, v56
	v_fmac_f32_e32 v153, v57, v57
	v_fmac_f32_e32 v150, v50, v50
	v_fmac_f32_e32 v151, v51, v51
	v_fmac_f32_e32 v152, v52, v52
	v_fmac_f32_e32 v153, v53, v53
	v_fmac_f32_e32 v150, v46, v46
	v_fmac_f32_e32 v151, v47, v47
	v_fmac_f32_e32 v152, v48, v48
	v_fmac_f32_e32 v153, v49, v49
	v_fmac_f32_e32 v150, v42, v42
	v_fmac_f32_e32 v151, v43, v43
	v_fmac_f32_e32 v152, v44, v44
	v_fmac_f32_e32 v153, v45, v45
	v_fmac_f32_e32 v150, v38, v38
	v_fmac_f32_e32 v151, v39, v39
	v_fmac_f32_e32 v152, v40, v40
	v_fmac_f32_e32 v153, v41, v41
	v_fmac_f32_e32 v150, v34, v34
	v_fmac_f32_e32 v151, v35, v35
	v_fmac_f32_e32 v152, v36, v36
	v_fmac_f32_e32 v153, v37, v37
	v_fmac_f32_e32 v150, v30, v30
	v_fmac_f32_e32 v151, v31, v31
	v_fmac_f32_e32 v152, v32, v32
	v_fmac_f32_e32 v153, v33, v33
	v_fmac_f32_e32 v150, v26, v26
	v_fmac_f32_e32 v151, v27, v27
	v_fmac_f32_e32 v152, v28, v28
	v_fmac_f32_e32 v153, v29, v29
	v_fmac_f32_e32 v150, v22, v22
	v_fmac_f32_e32 v151, v23, v23
	v_fmac_f32_e32 v152, v24, v24
	v_fmac_f32_e32 v153, v25, v25
	v_fmac_f32_e32 v150, v18, v18
	v_fmac_f32_e32 v151, v19, v19
	v_fmac_f32_e32 v152, v20, v20
	v_fmac_f32_e32 v153, v21, v21
	v_fmac_f32_e32 v150, v14, v14
	v_fmac_f32_e32 v151, v15, v15
	v_fmac_f32_e32 v152, v16, v16
	v_fmac_f32_e32 v153, v17, v17
	v_fmac_f32_e32 v150, v10, v10
	v_fmac_f32_e32 v151, v11, v11
	v_fmac_f32_e32 v152, v12, v12
	v_fmac_f32_e32 v153, v13, v13
	v_fmac_f32_e32 v150, v6, v6
	v_fmac_f32_e32 v151, v7, v7
	v_fmac_f32_e32 v152, v8, v8
	v_fmac_f32_e32 v153, v9, v9
	v_fmac_f32_e32 v150, v2, v2
	v_fmac_f32_e32 v151, v3, v3
	v_fmac_f32_e32 v152, v4, v4
	v_fmac_f32_e32 v153, v5, v5
	v_add_f32_e32 v150, v150, v151
	v_add_f32_e32 v152, v152, v153
	v_add_f32_e32 v150, v150, v152
	v_mbcnt_lo_u32_b32 v151, -1, 0
	v_mbcnt_hi_u32_b32 v151, -1, v151
	v_xor_b32_e32 v152, 16, v151
	v_lshlrev_b32_e32 v152, 2, v152
	ds_bpermute_b32 v152, v152, v150
	v_xor_b32_e32 v153, 32, v151
	v_lshlrev_b32_e32 v153, 2, v153
	s_waitcnt lgkmcnt(0)
	v_add_f32_e32 v150, v150, v152
	ds_bpermute_b32 v153, v153, v150
	v_add_u32_e32 v152, s24, v1
	v_lshlrev_b32_e32 v152, 2, v152
	v_add_u32_e32 v152, 0x11300, v152
	v_cmp_gt_u32_e32 vcc, 16, v1
	s_and_saveexec_b64 s[30:31], vcc
	s_waitcnt lgkmcnt(0)
	v_add_f32_e32 v150, v150, v153
	ds_write_b32 v152, v150
	s_mov_b64 exec, s[30:31]
	v_and_b32_e32 v138, 15, v0
	v_or_b32_e32 v134, s24, v138
	v_lshlrev_b32_e32 v135, 3, v1
	v_lshlrev_b32_e32 v139, 2, v1
	v_bfe_u32 v140, v0, 4, 2
	v_cmp_eq_u32_e64 s[2:3], 0, v1
